# v46 + late final combine (P15): the 8 per-wave {token positions, done flag} round trips issued together before the loop, read back from SGPRs
# speedup vs baseline: 1.0042x; 1.0042x over previous
.LBB0_2070:
	s_cmp_lt_i32 s92, 16
	s_cselect_b64 s[2:3], -1, 0
	s_and_b64 s[0:1], s[2:3], s[0:1]
	s_andn2_b64 vcc, exec, s[0:1]
	s_cbranch_vccnz .LBB0_2076
	s_add_u32 s3, s66, 0x420000
	s_addc_u32 s10, s67, 0
	s_add_u32 s11, s66, 0x460000
	s_addc_u32 s12, s67, 0
	s_add_u32 s13, s66, 0x40000
	s_addc_u32 s14, s67, 0
	s_lshl_b32 s0, s90, 3
	s_add_i32 s15, s0, s89
	s_add_i32 s0, 0, 0x23ab8
	s_lshl_b32 s16, s87, 3
	v_mov_b32_e32 v0, s0
	s_add_i32 s0, 0, 0x23abc
	ds_read_b32 v0, v0
	s_waitcnt lgkmcnt(0)
	v_mov_b32_e32 v1, s0
	s_add_i32 s0, 0, 0x23ac0
	s_abs_i32 s19, s16
	v_mov_b32_e32 v2, s0
	s_add_i32 s0, 0, 0x23ac4
	s_waitcnt vmcnt(0)
	v_cvt_f32_u32_e32 v16, s19
	ds_read_b32 v1, v1
	v_mov_b32_e32 v3, s0
	ds_read_b32 v2, v2
	ds_read_b32 v3, v3
	v_readfirstlane_b32 s0, v0
	v_mbcnt_lo_u32_b32 v0, -1, 0
	v_mbcnt_hi_u32_b32 v0, -1, v0
	v_rcp_iflag_f32_e32 v22, v16
	v_lshlrev_b32_e32 v0, 2, v0
	s_waitcnt lgkmcnt(2)
	v_readfirstlane_b32 s1, v1
	v_ashrrev_i32_e32 v1, 31, v0
	s_waitcnt lgkmcnt(1)
	v_readfirstlane_b32 s4, v2
	s_waitcnt lgkmcnt(0)
	v_readfirstlane_b32 s5, v3
	v_lshlrev_b64 v[4:5], 2, v[0:1]
	v_lshl_add_u64 v[18:19], s[0:1], 0, v[4:5]
	s_mov_b64 s[0:1], 0x2000
	v_lshl_add_u64 v[20:21], s[4:5], 0, v[4:5]
	v_mul_f32_e32 v22, 0x4f7ffffe, v22
	v_lshl_add_u64 v[2:3], v[18:19], 0, s[0:1]
	v_lshl_add_u64 v[4:5], v[20:21], 0, s[0:1]
	s_mov_b64 s[0:1], 0x3000
	v_cvt_u32_f32_e32 v22, v22
	v_lshl_add_u64 v[6:7], v[18:19], 0, s[0:1]
	v_lshl_add_u64 v[8:9], v[20:21], 0, s[0:1]
	s_mov_b64 s[0:1], 0x3400
	v_lshl_add_u64 v[10:11], v[18:19], 0, s[0:1]
	v_lshl_add_u64 v[12:13], v[20:21], 0, s[0:1]
	s_mov_b64 s[0:1], 0x3800
	v_lshl_add_u64 v[14:15], v[18:19], 0, s[0:1]
	v_lshl_add_u64 v[16:17], v[20:21], 0, s[0:1]
	s_mov_b64 s[0:1], 0x3c00
	v_lshl_add_u64 v[18:19], v[18:19], 0, s[0:1]
	v_lshl_add_u64 v[20:21], v[20:21], 0, s[0:1]
	s_sub_i32 s0, 0, s19
	v_readfirstlane_b32 s1, v22
	s_mul_i32 s0, s0, s1
	v_mbcnt_lo_u32_b32 v26, -1, 0
	s_mul_hi_u32 s0, s1, s0
	v_lshlrev_b64 v[24:25], 1, v[0:1]
	v_mbcnt_hi_u32_b32 v61, -1, v26
	s_add_i32 s20, s1, s0
	v_lshl_add_u64 v[22:23], s[76:77], 0, v[24:25]
	v_lshl_add_u64 v[24:25], s[66:67], 0, v[24:25]
	s_mov_b64 s[0:1], 0x45200000
	v_and_b32_e32 v26, 64, v61
	s_add_i32 s17, s87, 8
	s_mov_b32 s18, 0
	v_lshl_add_u64 v[24:25], v[24:25], 0, s[0:1]
	v_mov_b32_e32 v58, 0
	s_mov_b32 s2, 0x3fb504f3
	v_mov_b32_e32 v59, 0x3727c5ac
	s_mov_b32 s21, 0xf800000
	v_mov_b32_e32 v60, 0x260
	v_add_u32_e32 v62, 64, v26
	v_xor_b32_e32 v63, 1, v61
	v_xor_b32_e32 v64, 2, v61
	v_xor_b32_e32 v65, 4, v61
	v_xor_b32_e32 v66, 8, v61
	v_xor_b32_e32 v67, 16, v61
	v_xor_b32_e32 v68, 32, v61
	s_mov_b32 s48, s15
	s_mov_b32 s53, 0
	s_abs_i32 s49, s48
	s_mul_hi_u32 s50, s49, s20
	s_mul_i32 s50, s50, s19
	s_sub_i32 s49, s49, s50
	s_ashr_i32 s51, s48, 31
	s_sub_i32 s50, s49, s19
	s_cmp_ge_u32 s49, s19
	s_cselect_b32 s49, s50, s49
	s_sub_i32 s50, s49, s19
	s_cmp_ge_u32 s49, s19
	s_cselect_b32 s49, s50, s49
	s_xor_b32 s49, s49, s51
	s_sub_i32 s49, s49, s51
	s_add_i32 s52, s53, s49
	s_min_i32 s52, s52, 0x3fff
	s_max_i32 s52, s52, 0
	s_lshl_b32 s54, s52, 3
	s_add_u32 s54, s11, s54
	s_addc_u32 s55, s12, 0
	s_lshl_b32 s56, s52, 2
	s_add_u32 s56, s13, s56
	s_addc_u32 s57, s14, 0
	global_load_dwordx2 v[140:141], v58, s[54:55]
	global_load_dword v142, v58, s[56:57]
	s_add_i32 s48, s48, s17
	s_add_i32 s53, s53, s16
	s_abs_i32 s49, s48
	s_mul_hi_u32 s50, s49, s20
	s_mul_i32 s50, s50, s19
	s_sub_i32 s49, s49, s50
	s_ashr_i32 s51, s48, 31
	s_sub_i32 s50, s49, s19
	s_cmp_ge_u32 s49, s19
	s_cselect_b32 s49, s50, s49
	s_sub_i32 s50, s49, s19
	s_cmp_ge_u32 s49, s19
	s_cselect_b32 s49, s50, s49
	s_xor_b32 s49, s49, s51
	s_sub_i32 s49, s49, s51
	s_add_i32 s52, s53, s49
	s_min_i32 s52, s52, 0x3fff
	s_max_i32 s52, s52, 0
	s_lshl_b32 s54, s52, 3
	s_add_u32 s54, s11, s54
	s_addc_u32 s55, s12, 0
	s_lshl_b32 s56, s52, 2
	s_add_u32 s56, s13, s56
	s_addc_u32 s57, s14, 0
	global_load_dwordx2 v[144:145], v58, s[54:55]
	global_load_dword v146, v58, s[56:57]
	s_add_i32 s48, s48, s17
	s_add_i32 s53, s53, s16
	s_abs_i32 s49, s48
	s_mul_hi_u32 s50, s49, s20
	s_mul_i32 s50, s50, s19
	s_sub_i32 s49, s49, s50
	s_ashr_i32 s51, s48, 31
	s_sub_i32 s50, s49, s19
	s_cmp_ge_u32 s49, s19
	s_cselect_b32 s49, s50, s49
	s_sub_i32 s50, s49, s19
	s_cmp_ge_u32 s49, s19
	s_cselect_b32 s49, s50, s49
	s_xor_b32 s49, s49, s51
	s_sub_i32 s49, s49, s51
	s_add_i32 s52, s53, s49
	s_min_i32 s52, s52, 0x3fff
	s_max_i32 s52, s52, 0
	s_lshl_b32 s54, s52, 3
	s_add_u32 s54, s11, s54
	s_addc_u32 s55, s12, 0
	s_lshl_b32 s56, s52, 2
	s_add_u32 s56, s13, s56
	s_addc_u32 s57, s14, 0
	global_load_dwordx2 v[148:149], v58, s[54:55]
	global_load_dword v150, v58, s[56:57]
	s_add_i32 s48, s48, s17
	s_add_i32 s53, s53, s16
	s_abs_i32 s49, s48
	s_mul_hi_u32 s50, s49, s20
	s_mul_i32 s50, s50, s19
	s_sub_i32 s49, s49, s50
	s_ashr_i32 s51, s48, 31
	s_sub_i32 s50, s49, s19
	s_cmp_ge_u32 s49, s19
	s_cselect_b32 s49, s50, s49
	s_sub_i32 s50, s49, s19
	s_cmp_ge_u32 s49, s19
	s_cselect_b32 s49, s50, s49
	s_xor_b32 s49, s49, s51
	s_sub_i32 s49, s49, s51
	s_add_i32 s52, s53, s49
	s_min_i32 s52, s52, 0x3fff
	s_max_i32 s52, s52, 0
	s_lshl_b32 s54, s52, 3
	s_add_u32 s54, s11, s54
	s_addc_u32 s55, s12, 0
	s_lshl_b32 s56, s52, 2
	s_add_u32 s56, s13, s56
	s_addc_u32 s57, s14, 0
	global_load_dwordx2 v[152:153], v58, s[54:55]
	global_load_dword v154, v58, s[56:57]
	s_add_i32 s48, s48, s17
	s_add_i32 s53, s53, s16
	s_abs_i32 s49, s48
	s_mul_hi_u32 s50, s49, s20
	s_mul_i32 s50, s50, s19
	s_sub_i32 s49, s49, s50
	s_ashr_i32 s51, s48, 31
	s_sub_i32 s50, s49, s19
	s_cmp_ge_u32 s49, s19
	s_cselect_b32 s49, s50, s49
	s_sub_i32 s50, s49, s19
	s_cmp_ge_u32 s49, s19
	s_cselect_b32 s49, s50, s49
	s_xor_b32 s49, s49, s51
	s_sub_i32 s49, s49, s51
	s_add_i32 s52, s53, s49
	s_min_i32 s52, s52, 0x3fff
	s_max_i32 s52, s52, 0
	s_lshl_b32 s54, s52, 3
	s_add_u32 s54, s11, s54
	s_addc_u32 s55, s12, 0
	s_lshl_b32 s56, s52, 2
	s_add_u32 s56, s13, s56
	s_addc_u32 s57, s14, 0
	global_load_dwordx2 v[156:157], v58, s[54:55]
	global_load_dword v158, v58, s[56:57]
	s_add_i32 s48, s48, s17
	s_add_i32 s53, s53, s16
	s_abs_i32 s49, s48
	s_mul_hi_u32 s50, s49, s20
	s_mul_i32 s50, s50, s19
	s_sub_i32 s49, s49, s50
	s_ashr_i32 s51, s48, 31
	s_sub_i32 s50, s49, s19
	s_cmp_ge_u32 s49, s19
	s_cselect_b32 s49, s50, s49
	s_sub_i32 s50, s49, s19
	s_cmp_ge_u32 s49, s19
	s_cselect_b32 s49, s50, s49
	s_xor_b32 s49, s49, s51
	s_sub_i32 s49, s49, s51
	s_add_i32 s52, s53, s49
	s_min_i32 s52, s52, 0x3fff
	s_max_i32 s52, s52, 0
	s_lshl_b32 s54, s52, 3
	s_add_u32 s54, s11, s54
	s_addc_u32 s55, s12, 0
	s_lshl_b32 s56, s52, 2
	s_add_u32 s56, s13, s56
	s_addc_u32 s57, s14, 0
	global_load_dwordx2 v[160:161], v58, s[54:55]
	global_load_dword v162, v58, s[56:57]
	s_add_i32 s48, s48, s17
	s_add_i32 s53, s53, s16
	s_abs_i32 s49, s48
	s_mul_hi_u32 s50, s49, s20
	s_mul_i32 s50, s50, s19
	s_sub_i32 s49, s49, s50
	s_ashr_i32 s51, s48, 31
	s_sub_i32 s50, s49, s19
	s_cmp_ge_u32 s49, s19
	s_cselect_b32 s49, s50, s49
	s_sub_i32 s50, s49, s19
	s_cmp_ge_u32 s49, s19
	s_cselect_b32 s49, s50, s49
	s_xor_b32 s49, s49, s51
	s_sub_i32 s49, s49, s51
	s_add_i32 s52, s53, s49
	s_min_i32 s52, s52, 0x3fff
	s_max_i32 s52, s52, 0
	s_lshl_b32 s54, s52, 3
	s_add_u32 s54, s11, s54
	s_addc_u32 s55, s12, 0
	s_lshl_b32 s56, s52, 2
	s_add_u32 s56, s13, s56
	s_addc_u32 s57, s14, 0
	global_load_dwordx2 v[164:165], v58, s[54:55]
	global_load_dword v166, v58, s[56:57]
	s_add_i32 s48, s48, s17
	s_add_i32 s53, s53, s16
	s_abs_i32 s49, s48
	s_mul_hi_u32 s50, s49, s20
	s_mul_i32 s50, s50, s19
	s_sub_i32 s49, s49, s50
	s_ashr_i32 s51, s48, 31
	s_sub_i32 s50, s49, s19
	s_cmp_ge_u32 s49, s19
	s_cselect_b32 s49, s50, s49
	s_sub_i32 s50, s49, s19
	s_cmp_ge_u32 s49, s19
	s_cselect_b32 s49, s50, s49
	s_xor_b32 s49, s49, s51
	s_sub_i32 s49, s49, s51
	s_add_i32 s52, s53, s49
	s_min_i32 s52, s52, 0x3fff
	s_max_i32 s52, s52, 0
	s_lshl_b32 s54, s52, 3
	s_add_u32 s54, s11, s54
	s_addc_u32 s55, s12, 0
	s_lshl_b32 s56, s52, 2
	s_add_u32 s56, s13, s56
	s_addc_u32 s57, s14, 0
	global_load_dwordx2 v[168:169], v58, s[54:55]
	global_load_dword v170, v58, s[56:57]
	s_add_i32 s48, s48, s17
	s_add_i32 s53, s53, s16
	s_waitcnt vmcnt(0)
	v_readfirstlane_b32 s24, v140
	v_readfirstlane_b32 s25, v141
	v_readfirstlane_b32 s26, v142
	v_readfirstlane_b32 s27, v144
	v_readfirstlane_b32 s28, v145
	v_readfirstlane_b32 s29, v146
	v_readfirstlane_b32 s30, v148
	v_readfirstlane_b32 s31, v149
	v_readfirstlane_b32 s32, v150
	v_readfirstlane_b32 s33, v152
	v_readfirstlane_b32 s34, v153
	v_readfirstlane_b32 s35, v154
	v_readfirstlane_b32 s36, v156
	v_readfirstlane_b32 s37, v157
	v_readfirstlane_b32 s38, v158
	v_readfirstlane_b32 s39, v160
	v_readfirstlane_b32 s40, v161
	v_readfirstlane_b32 s41, v162
	v_readfirstlane_b32 s42, v164
	v_readfirstlane_b32 s43, v165
	v_readfirstlane_b32 s44, v166
	v_readfirstlane_b32 s45, v168
	v_readfirstlane_b32 s46, v169
	v_readfirstlane_b32 s47, v170
	s_branch .LBB0_2073
.LBB0_2072:
	s_mov_b32 s24, s27
	s_mov_b32 s25, s28
	s_mov_b32 s26, s29
	s_mov_b32 s27, s30
	s_mov_b32 s28, s31
	s_mov_b32 s29, s32
	s_mov_b32 s30, s33
	s_mov_b32 s31, s34
	s_mov_b32 s32, s35
	s_mov_b32 s33, s36
	s_mov_b32 s34, s37
	s_mov_b32 s35, s38
	s_mov_b32 s36, s39
	s_mov_b32 s37, s40
	s_mov_b32 s38, s41
	s_mov_b32 s39, s42
	s_mov_b32 s40, s43
	s_mov_b32 s41, s44
	s_mov_b32 s42, s45
	s_mov_b32 s43, s46
	s_mov_b32 s44, s47
	s_add_i32 s18, s18, s16
	s_add_i32 s15, s15, s17
	s_cmpk_lt_i32 s18, 0x4000
	s_cbranch_scc0 .LBB0_2076
.LBB0_2073:
	s_abs_i32 s1, s15
	s_mul_hi_u32 s4, s1, s20
	s_mul_i32 s4, s4, s19
	s_sub_i32 s1, s1, s4
	s_ashr_i32 s0, s15, 31
	s_sub_i32 s4, s1, s19
	s_cmp_ge_u32 s1, s19
	s_cselect_b32 s1, s4, s1
	s_sub_i32 s4, s1, s19
	s_cmp_ge_u32 s1, s19
	s_cselect_b32 s1, s4, s1
	s_xor_b32 s1, s1, s0
	s_sub_i32 s0, s1, s0
	s_add_i32 s4, s18, s0
	s_cmpk_gt_i32 s4, 0x3fff
	s_cbranch_scc1 .LBB0_2072
	s_lshl_b32 s0, s4, 1
	s_ashr_i32 s1, s0, 31
	s_lshl_b64 s[0:1], s[0:1], 2
	s_add_u32 s6, s11, s0
	s_addc_u32 s7, s12, s1
	s_ashr_i32 s5, s4, 31
	s_lshl_b64 s[8:9], s[4:5], 2
	s_add_u32 s8, s13, s8
	s_addc_u32 s9, s14, s9
	s_mov_b32 s8, s24
	s_cmp_lg_u32 s26, 0
	s_mov_b32 s6, s25
	s_cbranch_scc1 .LBB0_2072
	s_add_u32 s0, s3, s0
	s_addc_u32 s1, s10, s1
	s_lshl_b64 s[22:23], s[4:5], 12
	v_lshl_add_u64 v[28:29], v[22:23], 0, s[22:23]
	global_load_dwordx2 v[26:27], v[28:29], off
	global_load_dwordx2 v[30:31], v[28:29], off offset:512
	global_load_dwordx2 v[32:33], v[28:29], off offset:1024
	s_ashr_i32 s9, s8, 31
	s_ashr_i32 s7, s6, 31
	s_lshl_b64 s[8:9], s[8:9], 12
	s_lshl_b64 s[6:7], s[6:7], 12
	v_lshl_add_u64 v[34:35], v[24:25], 0, s[8:9]
	v_lshl_add_u64 v[38:39], v[24:25], 0, s[6:7]
	global_load_dwordx2 v[36:37], v[34:35], off
	global_load_dwordx2 v[40:41], v[38:39], off
	global_load_dwordx2 v[42:43], v[34:35], off offset:512
	global_load_dwordx2 v[44:45], v[38:39], off offset:512
	global_load_dwordx2 v[46:47], v[34:35], off offset:1024
	global_load_dwordx2 v[48:49], v[38:39], off offset:1024
	global_load_dwordx2 v[56:57], v58, s[0:1]
	global_load_dwordx2 v[50:51], v[28:29], off offset:1536
	global_load_dwordx2 v[52:53], v[34:35], off offset:1536
	global_load_dwordx2 v[54:55], v[38:39], off offset:1536
	global_load_dwordx2 v[70:71], v[28:29], off offset:2048
	global_load_dwordx2 v[72:73], v[28:29], off offset:2560
	global_load_dwordx2 v[74:75], v[28:29], off offset:3072
	global_load_dwordx2 v[76:77], v[34:35], off offset:2048
	global_load_dwordx2 v[78:79], v[34:35], off offset:2560
	global_load_dwordx2 v[80:81], v[34:35], off offset:3072
	global_load_dwordx2 v[82:83], v[38:39], off offset:2048
	global_load_dwordx2 v[84:85], v[38:39], off offset:2560
	global_load_dwordx2 v[86:87], v[38:39], off offset:3072
	global_load_dwordx2 v[88:89], v[28:29], off offset:3584
	global_load_dwordx2 v[90:91], v[34:35], off offset:3584
	v_cmp_lt_i32_e32 vcc, v63, v62
	s_waitcnt vmcnt(19)
	v_lshlrev_b32_e32 v96, 16, v40
	s_waitcnt vmcnt(18)
	v_lshlrev_b32_e32 v98, 16, v42
	v_and_b32_e32 v99, 0xffff0000, v42
	v_lshlrev_b32_e32 v42, 16, v43
	v_and_b32_e32 v43, 0xffff0000, v43
	s_waitcnt vmcnt(16)
	v_lshlrev_b32_e32 v102, 16, v46
	v_and_b32_e32 v103, 0xffff0000, v46
	s_waitcnt vmcnt(14)
	v_pk_mul_f32 v[42:43], v[56:57], v[42:43] op_sel_hi:[0,1]
	v_pk_mul_f32 v[102:103], v[56:57], v[102:103] op_sel_hi:[0,1]
	v_and_b32_e32 v97, 0xffff0000, v40
	v_lshlrev_b32_e32 v28, 16, v26
	v_lshlrev_b32_e32 v34, 16, v30
	v_and_b32_e32 v35, 0xffff0000, v30
	v_lshlrev_b32_e32 v30, 16, v31
	v_and_b32_e32 v31, 0xffff0000, v31
	v_lshlrev_b32_e32 v92, 16, v32
	v_and_b32_e32 v93, 0xffff0000, v32
	v_pk_fma_f32 v[30:31], v[30:31], s[2:3], v[42:43] op_sel_hi:[1,0,1]
	v_pk_fma_f32 v[42:43], v[92:93], s[2:3], v[102:103] op_sel_hi:[1,0,1]
	global_load_dwordx2 v[92:93], v[38:39], off offset:3584
	v_lshlrev_b32_e32 v94, 16, v36
	v_and_b32_e32 v95, 0xffff0000, v36
	v_and_b32_e32 v29, 0xffff0000, v26
	v_lshlrev_b32_e32 v36, 16, v37
	v_and_b32_e32 v37, 0xffff0000, v37
	v_pk_mul_f32 v[94:95], v[56:57], v[94:95] op_sel_hi:[0,1]
	v_lshlrev_b32_e32 v26, 16, v27
	v_and_b32_e32 v27, 0xffff0000, v27
	v_lshlrev_b32_e32 v100, 16, v44
	v_and_b32_e32 v101, 0xffff0000, v44
	v_lshlrev_b32_e32 v44, 16, v45
	v_and_b32_e32 v45, 0xffff0000, v45
	v_lshlrev_b32_e32 v46, 16, v47
	v_and_b32_e32 v47, 0xffff0000, v47
	v_lshlrev_b32_e32 v104, 16, v48
	v_and_b32_e32 v105, 0xffff0000, v48
	v_pk_mul_f32 v[36:37], v[56:57], v[36:37] op_sel_hi:[0,1]
	v_pk_fma_f32 v[28:29], v[28:29], s[2:3], v[94:95] op_sel_hi:[1,0,1]
	v_lshlrev_b32_e32 v32, 16, v33
	v_and_b32_e32 v33, 0xffff0000, v33
	v_lshlrev_b32_e32 v40, 16, v41
	v_and_b32_e32 v41, 0xffff0000, v41
	v_pk_mul_f32 v[46:47], v[56:57], v[46:47] op_sel_hi:[0,1]
	v_pk_fma_f32 v[26:27], v[26:27], s[2:3], v[36:37] op_sel_hi:[1,0,1]
	v_pk_fma_f32 v[36:37], v[56:57], v[96:97], v[28:29] op_sel:[1,0,0]
	v_pk_fma_f32 v[30:31], v[56:57], v[44:45], v[30:31] op_sel:[1,0,0]
	v_pk_fma_f32 v[28:29], v[56:57], v[104:105], v[42:43] op_sel:[1,0,0]
	s_waitcnt vmcnt(13)
	v_lshlrev_b32_e32 v42, 16, v52
	v_and_b32_e32 v43, 0xffff0000, v52
	v_lshlrev_b32_e32 v44, 16, v53
	v_and_b32_e32 v45, 0xffff0000, v53
	v_lshlrev_b32_e32 v48, 16, v49
	v_and_b32_e32 v49, 0xffff0000, v49
	v_pk_fma_f32 v[46:47], v[32:33], s[2:3], v[46:47] op_sel_hi:[1,0,1]
	v_pk_fma_f32 v[32:33], v[56:57], v[40:41], v[26:27] op_sel:[1,0,0]
	v_lshlrev_b32_e32 v40, 16, v50
	v_and_b32_e32 v41, 0xffff0000, v50
	v_lshlrev_b32_e32 v38, 16, v51
	v_and_b32_e32 v39, 0xffff0000, v51
	v_pk_mul_f32 v[44:45], v[56:57], v[44:45] op_sel_hi:[0,1]
	v_pk_mul_f32 v[42:43], v[56:57], v[42:43] op_sel_hi:[0,1]
	v_pk_fma_f32 v[26:27], v[56:57], v[48:49], v[46:47] op_sel:[1,0,0]
	s_waitcnt vmcnt(12)
	v_lshlrev_b32_e32 v46, 16, v54
	v_and_b32_e32 v47, 0xffff0000, v54
	v_lshlrev_b32_e32 v48, 16, v55
	v_and_b32_e32 v49, 0xffff0000, v55
	v_pk_fma_f32 v[40:41], v[40:41], s[2:3], v[42:43] op_sel_hi:[1,0,1]
	v_pk_fma_f32 v[38:39], v[38:39], s[2:3], v[44:45] op_sel_hi:[1,0,1]
	v_pk_fma_f32 v[40:41], v[56:57], v[46:47], v[40:41] op_sel:[1,0,0]
	v_pk_fma_f32 v[38:39], v[56:57], v[48:49], v[38:39] op_sel:[1,0,0]
	s_waitcnt vmcnt(8)
	v_lshlrev_b32_e32 v46, 16, v76
	v_and_b32_e32 v47, 0xffff0000, v76
	v_lshlrev_b32_e32 v48, 16, v77
	v_and_b32_e32 v49, 0xffff0000, v77
	v_lshlrev_b32_e32 v42, 16, v70
	v_and_b32_e32 v43, 0xffff0000, v70
	v_lshlrev_b32_e32 v44, 16, v71
	v_and_b32_e32 v45, 0xffff0000, v71
	v_pk_mul_f32 v[48:49], v[56:57], v[48:49] op_sel_hi:[0,1]
	v_pk_mul_f32 v[46:47], v[56:57], v[46:47] op_sel_hi:[0,1]
	s_waitcnt vmcnt(5)
	v_lshlrev_b32_e32 v50, 16, v82
	v_and_b32_e32 v51, 0xffff0000, v82
	v_lshlrev_b32_e32 v52, 16, v83
	v_and_b32_e32 v53, 0xffff0000, v83
	v_pk_fma_f32 v[46:47], v[42:43], s[2:3], v[46:47] op_sel_hi:[1,0,1]
	v_pk_fma_f32 v[42:43], v[44:45], s[2:3], v[48:49] op_sel_hi:[1,0,1]
	v_pk_fma_f32 v[44:45], v[56:57], v[50:51], v[46:47] op_sel:[1,0,0]
	v_pk_fma_f32 v[42:43], v[56:57], v[52:53], v[42:43] op_sel:[1,0,0]
	v_lshlrev_b32_e32 v50, 16, v78
	v_and_b32_e32 v51, 0xffff0000, v78
	v_lshlrev_b32_e32 v52, 16, v79
	v_and_b32_e32 v53, 0xffff0000, v79
	v_lshlrev_b32_e32 v46, 16, v72
	v_and_b32_e32 v47, 0xffff0000, v72
	v_lshlrev_b32_e32 v48, 16, v73
	v_and_b32_e32 v49, 0xffff0000, v73
	v_pk_mul_f32 v[52:53], v[56:57], v[52:53] op_sel_hi:[0,1]
	v_pk_mul_f32 v[50:51], v[56:57], v[50:51] op_sel_hi:[0,1]
	s_waitcnt vmcnt(4)
	v_lshlrev_b32_e32 v54, 16, v84
	v_and_b32_e32 v55, 0xffff0000, v84
	v_lshlrev_b32_e32 v70, 16, v85
	v_and_b32_e32 v71, 0xffff0000, v85
	v_pk_fma_f32 v[50:51], v[46:47], s[2:3], v[50:51] op_sel_hi:[1,0,1]
	v_pk_fma_f32 v[46:47], v[48:49], s[2:3], v[52:53] op_sel_hi:[1,0,1]
	v_pk_fma_f32 v[48:49], v[56:57], v[54:55], v[50:51] op_sel:[1,0,0]
	v_pk_fma_f32 v[46:47], v[56:57], v[70:71], v[46:47] op_sel:[1,0,0]
	v_lshlrev_b32_e32 v54, 16, v80
	v_and_b32_e32 v55, 0xffff0000, v80
	v_lshlrev_b32_e32 v70, 16, v81
	v_and_b32_e32 v71, 0xffff0000, v81
	v_lshlrev_b32_e32 v50, 16, v74
	v_and_b32_e32 v51, 0xffff0000, v74
	v_lshlrev_b32_e32 v52, 16, v75
	v_and_b32_e32 v53, 0xffff0000, v75
	v_pk_mul_f32 v[70:71], v[56:57], v[70:71] op_sel_hi:[0,1]
	v_pk_mul_f32 v[54:55], v[56:57], v[54:55] op_sel_hi:[0,1]
	s_waitcnt vmcnt(3)
	v_lshlrev_b32_e32 v72, 16, v86
	v_and_b32_e32 v73, 0xffff0000, v86
	v_lshlrev_b32_e32 v74, 16, v87
	v_and_b32_e32 v75, 0xffff0000, v87
	v_pk_fma_f32 v[54:55], v[50:51], s[2:3], v[54:55] op_sel_hi:[1,0,1]
	v_pk_fma_f32 v[50:51], v[52:53], s[2:3], v[70:71] op_sel_hi:[1,0,1]
	v_pk_mul_f32 v[98:99], v[56:57], v[98:99] op_sel_hi:[0,1]
	v_pk_fma_f32 v[50:51], v[56:57], v[74:75], v[50:51] op_sel:[1,0,0]
	v_pk_fma_f32 v[52:53], v[56:57], v[72:73], v[54:55] op_sel:[1,0,0]
	s_waitcnt vmcnt(1)
	v_lshlrev_b32_e32 v72, 16, v90
	v_and_b32_e32 v73, 0xffff0000, v90
	v_lshlrev_b32_e32 v74, 16, v91
	v_and_b32_e32 v75, 0xffff0000, v91
	v_pk_fma_f32 v[34:35], v[34:35], s[2:3], v[98:99] op_sel_hi:[1,0,1]
	v_lshlrev_b32_e32 v54, 16, v88
	v_and_b32_e32 v55, 0xffff0000, v88
	v_lshlrev_b32_e32 v70, 16, v89
	v_and_b32_e32 v71, 0xffff0000, v89
	v_pk_mul_f32 v[74:75], v[56:57], v[74:75] op_sel_hi:[0,1]
	v_pk_mul_f32 v[72:73], v[56:57], v[72:73] op_sel_hi:[0,1]
	v_pk_fma_f32 v[34:35], v[56:57], v[100:101], v[34:35] op_sel:[1,0,0]
	s_waitcnt vmcnt(0)
	v_lshlrev_b32_e32 v76, 16, v92
	v_and_b32_e32 v77, 0xffff0000, v92
	v_lshlrev_b32_e32 v78, 16, v93
	v_and_b32_e32 v79, 0xffff0000, v93
	v_pk_fma_f32 v[72:73], v[54:55], s[2:3], v[72:73] op_sel_hi:[1,0,1]
	v_pk_fma_f32 v[54:55], v[70:71], s[2:3], v[74:75] op_sel_hi:[1,0,1]
	v_mov_b32_e32 v70, v36
	v_pk_fma_f32 v[54:55], v[56:57], v[78:79], v[54:55] op_sel:[1,0,0]
	v_pk_fma_f32 v[56:57], v[56:57], v[76:77], v[72:73] op_sel:[1,0,0]
	v_mov_b32_e32 v71, v34
	v_mov_b32_e32 v72, v37
	v_mov_b32_e32 v73, v35
	v_pk_add_f32 v[70:71], v[70:71], v[72:73]
	v_mov_b32_e32 v72, v32
	v_mov_b32_e32 v73, v30
	v_mov_b32_e32 v74, v33
	v_mov_b32_e32 v75, v31
	v_pk_add_f32 v[72:73], v[72:73], v[74:75]
	v_mov_b32_e32 v74, v28
	v_pk_add_f32 v[70:71], v[70:71], v[72:73]
	v_pk_mov_b32 v[72:73], v[28:29], v[26:27] op_sel:[1,0]
	v_mov_b32_e32 v75, v27
	v_pk_add_f32 v[72:73], v[72:73], v[74:75]
	v_add_f32_e32 v69, 0, v70
	v_pk_add_f32 v[72:73], v[72:73], v[72:73] op_sel:[0,1] op_sel_hi:[1,0]
	v_add_f32_e32 v70, v69, v71
	v_add_f32_e32 v74, v40, v41
	v_add_f32_e32 v76, v38, v39
	v_mov_b32_e32 v71, v44
	v_mov_b32_e32 v73, v45
	v_mov_b32_e32 v75, v42
	v_mov_b32_e32 v77, v43
	v_pk_add_f32 v[70:71], v[70:71], v[72:73]
	v_pk_add_f32 v[72:73], v[74:75], v[76:77]
	v_mov_b32_e32 v74, v48
	v_pk_add_f32 v[70:71], v[70:71], v[72:73]
	v_pk_mov_b32 v[72:73], v[48:49], v[46:47] op_sel:[1,0]
	v_mov_b32_e32 v75, v47
	v_pk_add_f32 v[72:73], v[72:73], v[74:75]
	v_pk_add_f32 v[70:71], v[70:71], v[70:71] op_sel:[0,1] op_sel_hi:[1,0]
	v_pk_add_f32 v[72:73], v[72:73], v[72:73] op_sel:[0,1] op_sel_hi:[1,0]
	v_add_f32_e32 v74, v52, v53
	v_add_f32_e32 v76, v50, v51
	v_mov_b32_e32 v71, v56
	v_mov_b32_e32 v73, v57
	v_mov_b32_e32 v75, v54
	v_mov_b32_e32 v77, v55
	v_pk_add_f32 v[70:71], v[70:71], v[72:73]
	v_pk_add_f32 v[72:73], v[74:75], v[76:77]
	s_nop 0
	v_pk_add_f32 v[70:71], v[70:71], v[72:73]
	s_nop 0
	v_add_f32_e32 v69, v70, v71
	v_cndmask_b32_e32 v70, v61, v63, vcc
	v_lshlrev_b32_e32 v78, 2, v70
	s_nop 1
	v_mov_b32_dpp v70, v69 quad_perm:[1,0,3,2] row_mask:0xf bank_mask:0xf
	v_cmp_lt_i32_e32 vcc, v64, v62
	s_waitcnt lgkmcnt(0)
	v_add_f32_e32 v69, v69, v70
	v_cndmask_b32_e32 v70, v61, v64, vcc
	v_lshlrev_b32_e32 v86, 2, v70
	s_nop 1
	v_mov_b32_dpp v70, v69 quad_perm:[2,3,0,1] row_mask:0xf bank_mask:0xf
	v_cmp_lt_i32_e32 vcc, v65, v62
	s_waitcnt lgkmcnt(0)
	v_add_f32_e32 v69, v69, v70
	v_cndmask_b32_e32 v70, v61, v65, vcc
	v_lshlrev_b32_e32 v102, 2, v70
	s_nop 1
	v_mov_b32_dpp v70, v69 row_half_mirror row_mask:0xf bank_mask:0xf
	v_cmp_lt_i32_e32 vcc, v66, v62
	s_waitcnt lgkmcnt(0)
	v_add_f32_e32 v69, v69, v70
	v_cndmask_b32_e32 v70, v61, v66, vcc
	v_lshlrev_b32_e32 v118, 2, v70
	s_nop 1
	v_mov_b32_dpp v70, v69 row_mirror row_mask:0xf bank_mask:0xf
	v_cmp_lt_i32_e32 vcc, v67, v62
	s_waitcnt lgkmcnt(0)
	v_add_f32_e32 v69, v69, v70
	v_cndmask_b32_e32 v70, v61, v67, vcc
	v_lshlrev_b32_e32 v134, 2, v70
	v_mov_b32_e32 v70, v69
	s_nop 1
	v_permlane16_swap_b32_e32 v70, v69
	v_cmp_lt_i32_e32 vcc, v68, v62
	s_waitcnt lgkmcnt(0)
	v_add_f32_e32 v69, v69, v70
	v_cndmask_b32_e32 v70, v61, v68, vcc
	v_lshlrev_b32_e32 v135, 2, v70
	v_mov_b32_e32 v70, v69
	s_nop 1
	v_permlane32_swap_b32_e32 v70, v69
	s_waitcnt lgkmcnt(0)
	v_add_f32_e32 v69, v69, v70
	v_fmamk_f32 v37, v69, 0xba000000, v37
	v_fmamk_f32 v35, v69, 0xba000000, v35
	v_fmamk_f32 v33, v69, 0xba000000, v33
	v_fmac_f32_e32 v36, 0xba000000, v69
	v_fmamk_f32 v31, v69, 0xba000000, v31
	v_fmac_f32_e32 v34, 0xba000000, v69
	v_mov_b32_e32 v72, v37
	v_mov_b32_e32 v73, v35
	v_fmac_f32_e32 v32, 0xba000000, v69
	v_fmac_f32_e32 v30, 0xba000000, v69
	v_mov_b32_e32 v70, v36
	v_mov_b32_e32 v71, v34
	v_pk_mul_f32 v[72:73], v[72:73], v[72:73]
	v_mov_b32_e32 v74, v33
	v_mov_b32_e32 v75, v31
	v_pk_fma_f32 v[70:71], v[70:71], v[70:71], v[72:73]
	v_mov_b32_e32 v72, v32
	v_mov_b32_e32 v73, v30
	v_pk_mul_f32 v[74:75], v[74:75], v[74:75]
	v_fmamk_f32 v29, v69, 0xba000000, v29
	v_pk_fma_f32 v[72:73], v[72:73], v[72:73], v[74:75]
	v_fmac_f32_e32 v28, 0xba000000, v69
	v_pk_add_f32 v[70:71], v[70:71], v[72:73]
	v_fmamk_f32 v27, v69, 0xba000000, v27
	v_fmac_f32_e32 v26, 0xba000000, v69
	v_pk_add_f32 v[70:71], v[70:71], v[70:71] op_sel_hi:[0,1]
	v_pk_mul_f32 v[72:73], v[26:27], v[26:27]
	v_pk_mul_f32 v[74:75], v[28:29], v[28:29]
	v_fmac_f32_e32 v40, 0xba000000, v69
	v_pk_mov_b32 v[76:77], v[74:75], v[72:73] op_sel:[1,0]
	v_mov_b32_e32 v75, v73
	v_fmamk_f32 v41, v69, 0xba000000, v41
	v_fmac_f32_e32 v38, 0xba000000, v69
	v_mul_f32_e32 v70, v40, v40
	v_pk_add_f32 v[72:73], v[76:77], v[74:75]
	v_fmamk_f32 v39, v69, 0xba000000, v39
	v_pk_fma_f32 v[74:75], v[40:41], v[40:41], v[70:71] op_sel_hi:[1,1,0]
	v_mul_f32_e32 v70, v38, v38
	v_pk_add_f32 v[72:73], v[72:73], v[72:73] op_sel_hi:[0,1]
	v_pk_fma_f32 v[76:77], v[38:39], v[38:39], v[70:71] op_sel_hi:[1,1,0]
	v_fmamk_f32 v43, v69, 0xba000000, v43
	v_fmac_f32_e32 v42, 0xba000000, v69
	v_fmamk_f32 v45, v69, 0xba000000, v45
	v_fmac_f32_e32 v44, 0xba000000, v69
	v_mul_f32_e32 v74, v44, v44
	v_mul_f32_e32 v76, v45, v45
	v_mul_f32_e32 v72, v42, v42
	v_mul_f32_e32 v70, v43, v43
	v_pk_add_f32 v[74:75], v[74:75], v[76:77]
	v_pk_add_f32 v[70:71], v[72:73], v[70:71]
	v_fmamk_f32 v49, v69, 0xba000000, v49
	v_pk_add_f32 v[70:71], v[74:75], v[70:71]
	v_fmac_f32_e32 v48, 0xba000000, v69
	v_fmamk_f32 v47, v69, 0xba000000, v47
	v_fmac_f32_e32 v46, 0xba000000, v69
	v_pk_add_f32 v[70:71], v[70:71], v[70:71] op_sel_hi:[0,1]
	v_pk_mul_f32 v[72:73], v[46:47], v[46:47]
	v_pk_mul_f32 v[74:75], v[48:49], v[48:49]
	v_fmac_f32_e32 v52, 0xba000000, v69
	v_pk_mov_b32 v[76:77], v[74:75], v[72:73] op_sel:[1,0]
	v_mov_b32_e32 v75, v73
	v_fmamk_f32 v53, v69, 0xba000000, v53
	v_fmac_f32_e32 v50, 0xba000000, v69
	v_mul_f32_e32 v70, v52, v52
	v_pk_add_f32 v[72:73], v[76:77], v[74:75]
	v_fmamk_f32 v51, v69, 0xba000000, v51
	v_pk_fma_f32 v[74:75], v[52:53], v[52:53], v[70:71] op_sel_hi:[1,1,0]
	v_mul_f32_e32 v70, v50, v50
	v_pk_add_f32 v[72:73], v[72:73], v[72:73] op_sel_hi:[0,1]
	v_pk_fma_f32 v[76:77], v[50:51], v[50:51], v[70:71] op_sel_hi:[1,1,0]
	v_fmamk_f32 v55, v69, 0xba000000, v55
	v_fmac_f32_e32 v54, 0xba000000, v69
	v_fmamk_f32 v57, v69, 0xba000000, v57
	v_fmac_f32_e32 v56, 0xba000000, v69
	v_mul_f32_e32 v74, v56, v56
	v_mul_f32_e32 v76, v57, v57
	v_mul_f32_e32 v72, v54, v54
	v_mul_f32_e32 v70, v55, v55
	v_pk_add_f32 v[74:75], v[74:75], v[76:77]
	v_pk_add_f32 v[70:71], v[72:73], v[70:71]
	s_nop 0
	v_pk_add_f32 v[70:71], v[74:75], v[70:71]
	s_nop 0
	v_add_f32_e32 v69, v70, v71
	s_nop 1
	v_mov_b32_dpp v78, v69 quad_perm:[1,0,3,2] row_mask:0xf bank_mask:0xf
	global_load_dwordx4 v[70:73], v[2:3], off
	global_load_dwordx4 v[74:77], v[4:5], off
	s_waitcnt lgkmcnt(0)
	v_add_f32_e32 v69, v69, v78
	s_nop 1
	v_mov_b32_dpp v94, v69 quad_perm:[2,3,0,1] row_mask:0xf bank_mask:0xf
	global_load_dwordx4 v[78:81], v[2:3], off offset:1024
	global_load_dwordx4 v[82:85], v[4:5], off offset:1024
	global_load_dwordx4 v[86:89], v[2:3], off offset:2048
	global_load_dwordx4 v[90:93], v[4:5], off offset:2048
	s_waitcnt lgkmcnt(0)
	v_add_f32_e32 v69, v69, v94
	s_nop 1
	v_mov_b32_dpp v110, v69 row_half_mirror row_mask:0xf bank_mask:0xf
	global_load_dwordx4 v[94:97], v[2:3], off offset:3072
	global_load_dwordx4 v[98:101], v[4:5], off offset:3072
	global_load_dwordx4 v[102:105], v[6:7], off
	global_load_dwordx4 v[106:109], v[8:9], off
	s_waitcnt lgkmcnt(0)
	v_add_f32_e32 v69, v69, v110
	s_nop 1
	v_mov_b32_dpp v126, v69 row_mirror row_mask:0xf bank_mask:0xf
	global_load_dwordx4 v[110:113], v[10:11], off
	global_load_dwordx4 v[114:117], v[12:13], off
	global_load_dwordx4 v[118:121], v[14:15], off
	global_load_dwordx4 v[122:125], v[16:17], off
	s_waitcnt lgkmcnt(0)
	v_add_f32_e32 v69, v69, v126
	global_load_dwordx4 v[126:129], v[18:19], off
	global_load_dwordx4 v[130:133], v[20:21], off
	v_mov_b32_e32 v134, v69
	s_nop 1
	v_permlane16_swap_b32_e32 v134, v69
	s_waitcnt lgkmcnt(0)
	v_add_f32_e32 v69, v69, v134
	v_mov_b32_e32 v134, v69
	s_nop 1
	v_permlane32_swap_b32_e32 v134, v69
	s_waitcnt lgkmcnt(0)
	v_add_f32_e32 v69, v69, v134
	v_fmamk_f32 v69, v69, 0x3a000000, v59
	v_mul_f32_e32 v134, 0x4f800000, v69
	v_cmp_gt_f32_e32 vcc, s21, v69
	s_nop 1
	v_cndmask_b32_e32 v69, v69, v134, vcc
	v_sqrt_f32_e32 v134, v69
	s_nop 0
	v_add_u32_e32 v135, -1, v134
	v_fma_f32 v136, -v135, v134, v69
	v_cmp_ge_f32_e64 s[0:1], 0, v136
	v_add_u32_e32 v136, 1, v134
	s_nop 0
	v_cndmask_b32_e64 v135, v134, v135, s[0:1]
	v_fma_f32 v134, -v136, v134, v69
	v_cmp_lt_f32_e64 s[0:1], 0, v134
	s_nop 1
	v_cndmask_b32_e64 v134, v135, v136, s[0:1]
	v_mul_f32_e32 v135, 0x37800000, v134
	v_cndmask_b32_e32 v134, v134, v135, vcc
	v_cmp_class_f32_e32 vcc, v69, v60
	s_nop 1
	v_cndmask_b32_e32 v69, v134, v69, vcc
	v_div_scale_f32 v134, s[0:1], v69, v69, 1.0
	v_rcp_f32_e32 v135, v134
	s_lshl_b64 s[0:1], s[4:5], 13
	s_add_u32 s0, s64, s0
	s_addc_u32 s1, s65, s1
	v_fma_f32 v136, -v134, v135, 1.0
	v_fmac_f32_e32 v135, v136, v135
	v_div_scale_f32 v136, vcc, 1.0, v69, 1.0
	v_mul_f32_e32 v137, v136, v135
	v_fma_f32 v138, -v134, v137, v136
	v_fmac_f32_e32 v137, v138, v135
	v_fma_f32 v134, -v134, v137, v136
	v_div_fmas_f32 v134, v134, v135, v137
	v_div_fixup_f32 v134, v134, v69, 1.0
	v_pk_mul_f32 v[32:33], v[32:33], v[134:135] op_sel_hi:[1,0]
	v_pk_mul_f32 v[34:35], v[34:35], v[134:135] op_sel_hi:[1,0]
	v_pk_mul_f32 v[30:31], v[30:31], v[134:135] op_sel_hi:[1,0]
	v_pk_mul_f32 v[36:37], v[36:37], v[134:135] op_sel_hi:[1,0]
	s_waitcnt vmcnt(14)
	v_pk_fma_f32 v[72:73], v[72:73], v[32:33], v[76:77]
	v_pk_mul_f32 v[26:27], v[26:27], v[134:135] op_sel_hi:[1,0]
	v_pk_fma_f32 v[70:71], v[70:71], v[36:37], v[74:75]
	s_waitcnt vmcnt(12)
	v_pk_fma_f32 v[32:33], v[80:81], v[30:31], v[84:85]
	v_pk_fma_f32 v[30:31], v[78:79], v[34:35], v[82:83]
	v_pk_mul_f32 v[34:35], v[28:29], v[134:135] op_sel_hi:[1,0]
	s_waitcnt vmcnt(10)
	v_pk_fma_f32 v[28:29], v[88:89], v[26:27], v[92:93]
	v_pk_fma_f32 v[26:27], v[86:87], v[34:35], v[90:91]
	v_pk_mul_f32 v[34:35], v[40:41], v[134:135] op_sel_hi:[1,0]
	v_pk_mul_f32 v[36:37], v[38:39], v[134:135] op_sel_hi:[1,0]
	v_pk_mul_f32 v[38:39], v[44:45], v[134:135] op_sel_hi:[1,0]
	v_pk_mul_f32 v[44:45], v[46:47], v[134:135] op_sel_hi:[1,0]
	v_pk_mul_f32 v[46:47], v[52:53], v[134:135] op_sel_hi:[1,0]
	v_pk_mul_f32 v[52:53], v[54:55], v[134:135] op_sel_hi:[1,0]
	v_lshl_add_u64 v[54:55], v[0:1], 2, s[0:1]
	s_waitcnt vmcnt(8)
	v_pk_fma_f32 v[36:37], v[96:97], v[36:37], v[100:101]
	v_pk_fma_f32 v[34:35], v[94:95], v[34:35], v[98:99]
	v_pk_mul_f32 v[40:41], v[42:43], v[134:135] op_sel_hi:[1,0]
	global_store_dwordx4 v[54:55], v[70:73], off
	global_store_dwordx4 v[54:55], v[30:33], off offset:1024
	global_store_dwordx4 v[54:55], v[26:29], off offset:2048
	global_store_dwordx4 v[54:55], v[34:37], off offset:3072
	s_waitcnt vmcnt(10)
	v_pk_fma_f32 v[40:41], v[104:105], v[40:41], v[108:109]
	v_add_co_u32_e32 v26, vcc, 0x1000, v54
	v_pk_fma_f32 v[38:39], v[102:103], v[38:39], v[106:107]
	v_pk_mul_f32 v[42:43], v[48:49], v[134:135] op_sel_hi:[1,0]
	v_pk_mul_f32 v[48:49], v[50:51], v[134:135] op_sel_hi:[1,0]
	v_pk_mul_f32 v[50:51], v[56:57], v[134:135] op_sel_hi:[1,0]
	v_addc_co_u32_e32 v27, vcc, 0, v55, vcc
	s_waitcnt vmcnt(8)
	v_pk_fma_f32 v[44:45], v[112:113], v[44:45], v[116:117]
	v_pk_fma_f32 v[42:43], v[110:111], v[42:43], v[114:115]
	s_waitcnt vmcnt(6)
	v_pk_fma_f32 v[48:49], v[120:121], v[48:49], v[124:125]
	v_pk_fma_f32 v[46:47], v[118:119], v[46:47], v[122:123]
	s_waitcnt vmcnt(4)
	v_pk_fma_f32 v[52:53], v[128:129], v[52:53], v[132:133]
	v_pk_fma_f32 v[50:51], v[126:127], v[50:51], v[130:131]
	global_store_dwordx4 v[26:27], v[38:41], off
	global_store_dwordx4 v[26:27], v[42:45], off offset:1024
	global_store_dwordx4 v[26:27], v[46:49], off offset:2048
	global_store_dwordx4 v[26:27], v[50:53], off offset:3072
	s_branch .LBB0_2072
